# v37 but the static prio of waves 4-7 is dropped after the MLA and GQA items (not kept for neighbourhood attention / idle conversion)
# speedup vs baseline: 1.0100x; 1.0100x over previous
.LBB0_643:
	s_setprio 0
	s_not_b32 s0, s41
	s_add_i32 s42, s46, s0
	s_mov_b64 s[0:1], -1
	s_cmpk_gt_i32 s42, 0x87
	s_waitcnt vmcnt(0)
	v_lshlrev_b32_e32 v172, 2, v184
	s_cbranch_scc0 .LBB0_720
	s_ashr_i32 s0, s47, 6
	s_lshl_b32 s1, s41, 3
	s_add_i32 s40, s1, s0
	s_add_u32 s41, s6, 0x17458000
	s_mulk_i32 s0, 0x2400
	s_addc_u32 s43, s7, 0
	s_add_i32 s0, s0, 0
	s_add_u32 s44, s6, 0x7458000
	s_addc_u32 s45, s7, 0
	s_add_u32 s47, s6, 0x6458000
	s_addc_u32 s48, s7, 0
	s_add_u32 s49, s6, 0x5458000
	s_addc_u32 s50, s7, 0
	s_add_u32 s51, s6, 0x4d58000
	s_addc_u32 s52, s7, 0
	s_add_u32 s53, s6, 0x158000
	s_addc_u32 s54, s7, 0
	s_add_u32 s55, s6, 0x3390c000
	v_lshlrev_b32_e32 v2, 4, v184
	s_addc_u32 s56, s7, 0
	v_lshlrev_b32_e32 v0, 2, v184
	v_and_b32_e32 v78, 48, v2
	s_add_u32 s57, s6, 0x35e0c000
	v_lshlrev_b32_e32 v2, 1, v184
	v_and_b32_e32 v82, 48, v184
	v_and_b32_e32 v0, 60, v0
	v_bfe_u32 v83, v184, 2, 4
	s_addc_u32 s58, s7, 0
	v_and_b32_e32 v2, 0x60, v2
	v_and_b32_e32 v8, 7, v184
	v_bfe_u32 v87, v184, 3, 3
	v_mov_b32_e32 v77, 0
	v_add_u32_e32 v1, s0, v82
	v_mul_u32_u24_e32 v3, 0x50, v0
	v_add_u32_e32 v4, s0, v78
	v_mul_u32_u24_e32 v5, 0x50, v83
	s_add_u32 s59, s6, 0x3760c000
	v_add_u32_e32 v6, s0, v2
	v_mul_u32_u24_e32 v7, 0x90, v0
	v_lshlrev_b32_e32 v2, 3, v8
	v_lshl_add_u32 v8, v8, 4, s0
	v_mul_u32_u24_e32 v9, 0x90, v87
	s_mul_i32 s40, s40, 9
	s_mov_b32 s1, 0
	v_mov_b32_e32 v79, v77
	v_or_b32_e32 v84, 16, v83
	v_or_b32_e32 v85, 32, v83
	v_or_b32_e32 v86, 48, v83
	s_addc_u32 s60, s7, 0
	v_or_b32_e32 v88, 8, v87
	v_or_b32_e32 v89, 16, v87
	v_or_b32_e32 v90, 24, v87
	v_or_b32_e32 v91, 32, v87
	v_or_b32_e32 v92, 40, v87
	v_or_b32_e32 v93, 48, v87
	v_or_b32_e32 v94, 56, v87
	s_mov_b32 s65, -9
	s_add_i32 s61, 0, 0x204f8
	s_movk_i32 s62, 0x2000
	s_movk_i32 s63, 0x4000
	s_movk_i32 s64, 0x6000
	s_mov_b32 s66, 0x12000
	s_mov_b32 s67, 0xc3e00000
	v_add_u32_e32 v95, v1, v3
	v_add_u32_e32 v96, v4, v5
	s_movk_i32 s68, 0x3000
	s_movk_i32 s69, 0x5000
	s_movk_i32 s70, 0x7000
	s_add_i32 s71, 0, 0x204c0
	s_add_i32 s72, 0, 0x204b8
	s_add_i32 s73, 0, 0x204b0
	s_add_i32 s74, 0, 0x204a8
	s_add_i32 s75, 0, 0x20458
	s_add_i32 s76, 0, 0x20448
	s_add_i32 s77, 0, 0x20440
	s_mov_b32 s78, 0x9000
	s_mov_b32 s79, 0x1b000
	s_mov_b32 s80, 0x25000
	s_mov_b32 s81, 0x2e000
	s_mov_b32 s82, 0x37000
	s_mov_b32 s83, 0x41000
	s_mov_b32 s84, 0x4a000
	s_mov_b32 s85, 0x53000
	s_mov_b32 s86, 0x5d000
	s_mov_b32 s87, 0x66000
	s_mov_b32 s88, 0x6f000
	s_mov_b32 s89, 0x79000
	s_mov_b32 s90, 0x82000
	s_mov_b32 s91, 0x8b000
	v_add_u32_e32 v97, v6, v7
	v_lshlrev_b32_e32 v76, 1, v2
	v_lshlrev_b32_e32 v80, 2, v0
	v_mov_b32_e32 v98, 0x43e00000
	v_mov_b32_e32 v100, v77
	v_mov_b32_e32 v101, v77
	v_mov_b32_e32 v102, v77
	v_mov_b32_e32 v103, v77
	v_add_u32_e32 v99, v8, v9
	s_branch .LBB0_647

.LBB0_1935:
	s_setprio 0
	s_not_b32 s0, s44
	s_add_i32 s40, s42, s0
	s_mov_b64 s[0:1], -1
	s_cmpk_gt_i32 s40, 0x7f
	v_lshlrev_b32_e32 v176, 2, v184
	s_cbranch_scc0 .LBB0_2012
	s_ashr_i32 s0, s45, 6
	s_lshl_b32 s1, s44, 3
	s_add_i32 s38, s1, s0
	s_add_u32 s41, s6, 0x17458000
	s_mulk_i32 s0, 0x2400
	s_addc_u32 s44, s7, 0
	s_add_i32 s0, s0, 0
	s_add_u32 s45, s6, 0x7458000
	s_addc_u32 s46, s7, 0
	s_add_u32 s47, s6, 0x6458000
	s_addc_u32 s48, s7, 0
	s_add_u32 s49, s6, 0x5458000
	s_addc_u32 s50, s7, 0
	s_add_u32 s51, s6, 0x4d58000
	s_addc_u32 s52, s7, 0
	s_add_u32 s53, s6, 0x158000
	s_addc_u32 s54, s7, 0
	s_add_u32 s55, s6, 0x3390c000
	v_lshlrev_b32_e32 v2, 4, v184
	s_addc_u32 s56, s7, 0
	v_lshlrev_b32_e32 v0, 2, v184
	v_and_b32_e32 v78, 48, v2
	s_add_u32 s57, s6, 0x35e0c000
	v_lshlrev_b32_e32 v2, 1, v184
	s_waitcnt vmcnt(33)
	v_and_b32_e32 v82, 48, v184
	v_and_b32_e32 v0, 60, v0
	v_bfe_u32 v83, v184, 2, 4
	s_addc_u32 s58, s7, 0
	v_and_b32_e32 v2, 0x60, v2
	v_and_b32_e32 v8, 7, v184
	s_waitcnt vmcnt(32)
	v_bfe_u32 v87, v184, 3, 3
	v_mov_b32_e32 v77, 0
	v_add_u32_e32 v1, s0, v82
	v_mul_u32_u24_e32 v3, 0x50, v0
	v_add_u32_e32 v4, s0, v78
	v_mul_u32_u24_e32 v5, 0x50, v83
	s_add_u32 s59, s6, 0x3760c000
	v_add_u32_e32 v6, s0, v2
	v_mul_u32_u24_e32 v7, 0x90, v0
	v_lshlrev_b32_e32 v2, 3, v8
	v_lshl_add_u32 v8, v8, 4, s0
	v_mul_u32_u24_e32 v9, 0x90, v87
	s_mul_i32 s38, s38, 9
	s_mov_b32 s1, 0
	v_mov_b32_e32 v79, v77
	v_or_b32_e32 v84, 16, v83
	v_or_b32_e32 v85, 32, v83
	v_or_b32_e32 v86, 48, v83
	s_addc_u32 s60, s7, 0
	v_or_b32_e32 v88, 8, v87
	v_or_b32_e32 v89, 16, v87
	v_or_b32_e32 v90, 24, v87
	v_or_b32_e32 v91, 32, v87
	v_or_b32_e32 v92, 40, v87
	v_or_b32_e32 v93, 48, v87
	v_or_b32_e32 v94, 56, v87
	s_mov_b32 s65, -9
	s_add_i32 s61, 0, 0x204f8
	s_movk_i32 s62, 0x2000
	s_movk_i32 s63, 0x4000
	s_movk_i32 s64, 0x6000
	s_mov_b32 s66, 0x12000
	s_mov_b32 s67, 0xc3e00000
	v_add_u32_e32 v95, v1, v3
	v_add_u32_e32 v96, v4, v5
	s_movk_i32 s68, 0x3000
	s_movk_i32 s69, 0x5000
	s_movk_i32 s70, 0x7000
	s_add_i32 s71, 0, 0x204c0
	s_add_i32 s72, 0, 0x204b8
	s_add_i32 s73, 0, 0x204b0
	s_add_i32 s74, 0, 0x204a8
	s_add_i32 s75, 0, 0x20458
	s_add_i32 s76, 0, 0x20448
	s_add_i32 s77, 0, 0x20440
	s_mov_b32 s78, 0x9000
	s_mov_b32 s79, 0x1b000
	s_mov_b32 s80, 0x25000
	s_mov_b32 s81, 0x2e000
	s_mov_b32 s82, 0x37000
	s_mov_b32 s83, 0x41000
	s_mov_b32 s84, 0x4a000
	s_mov_b32 s85, 0x53000
	s_mov_b32 s86, 0x5d000
	s_mov_b32 s87, 0x66000
	s_mov_b32 s88, 0x6f000
	s_mov_b32 s89, 0x79000
	s_mov_b32 s90, 0x82000
	s_mov_b32 s91, 0x8b000
	v_add_u32_e32 v97, v6, v7
	v_lshlrev_b32_e32 v76, 1, v2
	v_lshlrev_b32_e32 v80, 2, v0
	v_mov_b32_e32 v98, 0x43e00000
	v_mov_b32_e32 v100, v77
	v_mov_b32_e32 v101, v77
	v_mov_b32_e32 v102, v77
	v_mov_b32_e32 v103, v77
	v_add_u32_e32 v99, v8, v9
	s_branch .LBB0_1939
